# C6 K-loop restructured: one 64-MFMA segment per K-tile with A-half1 fragments read inside it, two barriers per K-tile instead of four; staging split between the wave halves
# baseline (speedup 1.0000x reference)
.LBB0_2616:
	s_add_u32 s12, s12, 0xac00000
	s_addc_u32 s13, s13, 0
	s_add_u32 s14, s14, 0x1f00000
	s_addc_u32 s15, s15, 0
	s_lshl_b32 s17, s17, 5
	s_and_b32 s21, s17, 0x60
	s_add_i32 m0, s36, 0x18000
	v_lshl_add_u64 v[8:9], v[8:9], 0, s[56:57]
	s_lshl_b32 s20, s16, 13
	s_lshl_b32 s17, s21, 7
	s_waitcnt vmcnt(2)
	s_barrier
	global_load_lds_dwordx4 v[8:9], off
	v_lshl_add_u64 v[6:7], v[6:7], 0, s[56:57]
	s_add_i32 m0, s36, 0x1a000
	s_add_i32 s44, s36, 0x8000
	s_add_i32 s45, s36, 0xa000
	global_load_lds_dwordx4 v[6:7], off
	v_lshl_add_u64 v[2:3], v[2:3], 0, s[56:57]
	s_mov_b32 m0, s44
	s_add_u32 s18, s6, 0x40080
	global_load_lds_dwordx4 v[2:3], off
	v_lshl_add_u64 v[2:3], v[4:5], 0, s[56:57]
	s_mov_b32 m0, s45
	s_addc_u32 s19, s7, 0
	global_load_lds_dwordx4 v[2:3], off
	s_add_i32 m0, s36, 0x1c000
	v_lshl_add_u64 v[2:3], s[18:19], 0, v[162:163]
	global_load_lds_dwordx4 v[2:3], off
	v_lshl_add_u64 v[2:3], s[18:19], 0, v[158:159]
	s_add_i32 m0, s36, 0x1e000
	s_cmpk_lt_u32 s4, 0x100
	global_load_lds_dwordx4 v[2:3], off
	v_lshrrev_b32_e32 v3, 1, v0
	v_and_b32_e32 v3, 24, v3
	v_and_b32_e32 v2, 15, v0
	v_lshlrev_b32_e32 v4, 1, v3
	v_lshlrev_b32_e32 v0, 2, v0
	v_lshl_or_b32 v180, s16, 6, v2
	v_lshl_or_b32 v2, v2, 6, v4
	v_and_b32_e32 v0, 32, v0
	v_bitop3_b32 v4, v2, s20, v0 bitop3:0xde
	v_bitop3_b32 v181, v2, s17, v0 bitop3:0xde
	v_lshlrev_b32_e32 v0, 14, v10
	v_and_b32_e32 v0, 0xffff8000, v0
	v_lshl_add_u32 v0, v11, 11, v0
	v_and_b32_e32 v2, 1, v10
	v_lshl_or_b32 v0, v2, 6, v0
	v_lshl_add_u32 v166, v12, 1, v0
	v_lshlrev_b32_e32 v0, 14, v14
	v_and_b32_e32 v0, 0xffff8000, v0
	s_waitcnt vmcnt(6)
	v_lshl_add_u32 v0, v13, 11, v0
	v_and_b32_e32 v2, 1, v14
	v_lshl_or_b32 v0, v2, 6, v0
	v_readlane_b32 s18, v254, 13
	s_cselect_b64 s[16:17], -1, 0
	v_or_b32_e32 v182, s21, v3
	v_mov_b32_e32 v167, v1
	v_lshl_add_u32 v168, v15, 1, v0
	v_mov_b32_e32 v169, v1
	s_mov_b32 s46, 0
	v_add_u32_e32 v183, 0, v4
	v_readlane_b32 s47, v253, 52
	s_mov_b32 s4, s18
	s_barrier
	v_readlane_b32 s19, v254, 14
	v_mov_b32_e32 v208, v162
	v_mov_b32_e32 v209, v158
	v_mov_b32_e32 v224, v164
	v_mov_b32_e32 v225, v160
	s_branch .LBB0_2619

.Lnobar_c6:
	v_add_u32_e32 v0, 0x10000, v181
	s_add_u32 s82, s41, 0xffffff00
	s_addc_u32 s83, s48, -1
	s_mov_b32 s84, s26
	s_mov_b32 s85, s27
	s_mov_b32 s49, 0
.LBB0_2626:
	s_add_u32 s82, s82, 0x80
	s_addc_u32 s83, s83, 0
	s_add_u32 s84, s84, 0x80
	s_addc_u32 s85, s85, 0
	ds_read_b128 v[130:133], v0
	ds_read_b128 v[134:137], v0 offset:1024
	ds_read_b128 v[138:141], v0 offset:2048
	ds_read_b128 v[142:145], v0 offset:3072
	ds_read_b128 v[146:149], v0 offset:16384
	ds_read_b128 v[150:153], v0 offset:17408
	ds_read_b128 v[154:157], v0 offset:18432
	ds_read_b128 v[170:173], v0 offset:19456
	ds_read_b128 v[174:177], v183
	ds_read_b128 v[184:187], v183 offset:1024
	ds_read_b128 v[188:191], v183 offset:2048
	ds_read_b128 v[192:195], v183 offset:3072
	ds_read_b128 v[196:199], v183 offset:4096
	ds_read_b128 v[200:203], v183 offset:5120
	ds_read_b128 v[204:207], v183 offset:6144
	ds_read_b128 v[216:219], v183 offset:7168
	s_and_b64 vcc, exec, s[16:17]
	s_cbranch_vccz .Lc6x_tr_a
	s_add_u32 s26, s82, 0x10000
	s_addc_u32 s27, s83, 0
	s_add_i32 m0, s36, 0x18000
	s_nop 0
	global_load_lds_dwordx4 v208, s[82:83]
	s_add_i32 m0, s36, 0x1a000
	s_nop 0
	global_load_lds_dwordx4 v209, s[82:83]
	s_add_i32 m0, s36, 0x19000
	s_nop 0
	global_load_lds_dwordx4 v208, s[26:27]
	s_add_i32 m0, s36, 0x1b000
	s_nop 0
	global_load_lds_dwordx4 v209, s[26:27]
	s_add_u32 s28, s82, 0x40000
	s_addc_u32 s29, s83, 0
	s_add_u32 s26, s28, 0x10000
	s_addc_u32 s27, s29, 0
	s_add_i32 m0, s36, 0x1c000
	s_nop 0
	global_load_lds_dwordx4 v208, s[28:29]
	s_add_i32 m0, s36, 0x1e000
	s_nop 0
	global_load_lds_dwordx4 v209, s[28:29]
	s_add_i32 m0, s36, 0x1d000
	s_nop 0
	global_load_lds_dwordx4 v208, s[26:27]
	s_add_i32 m0, s36, 0x1f000
	s_nop 0
	global_load_lds_dwordx4 v209, s[26:27]
	s_add_u32 s26, s84, 0x10000
	s_addc_u32 s27, s85, 0
	s_add_i32 m0, s36, 0x8000
	s_nop 0
	global_load_lds_dwordx4 v224, s[84:85]
	s_add_i32 m0, s36, 0xa000
	s_nop 0
	global_load_lds_dwordx4 v225, s[84:85]
	s_add_i32 m0, s36, 0x9000
	s_nop 0
	global_load_lds_dwordx4 v224, s[26:27]
	s_add_i32 m0, s36, 0xb000
	s_nop 0
	global_load_lds_dwordx4 v225, s[26:27]
	s_branch .Lc6x_st_a
.Lc6x_tr_a:
	s_add_u32 s28, s84, 0x40000
	s_addc_u32 s29, s85, 0
	s_add_u32 s26, s84, 0x30000
	s_addc_u32 s27, s85, 0
	s_add_i32 m0, s36, 0xc000
	s_nop 0
	global_load_lds_dwordx4 v224, s[28:29]
	s_add_i32 m0, s36, 0xe000
	s_nop 0
	global_load_lds_dwordx4 v225, s[28:29]
	s_add_i32 m0, s36, 0xb000
	s_nop 0
	global_load_lds_dwordx4 v224, s[26:27]
	s_add_i32 m0, s36, 0xd000
	s_nop 0
	global_load_lds_dwordx4 v225, s[26:27]
.Lc6x_st_a:
	s_waitcnt lgkmcnt(0)
	s_barrier
	ds_read_b128 v[158:161], v183 offset:16384
	ds_read_b128 v[162:165], v183 offset:18432
	ds_read_b128 v[166:169], v183 offset:20480
	ds_read_b128 v[220:223], v183 offset:22528
	s_setprio 1
	v_mfma_f32_16x16x32_bf16 v[126:129], v[130:133], v[174:177], v[126:129]
	v_mfma_f32_16x16x32_bf16 v[122:125], v[138:141], v[174:177], v[122:125]
	v_mfma_f32_16x16x32_bf16 v[110:113], v[130:133], v[188:191], v[110:113]
	v_mfma_f32_16x16x32_bf16 v[106:109], v[138:141], v[188:191], v[106:109]
	v_mfma_f32_16x16x32_bf16 v[94:97], v[130:133], v[196:199], v[94:97]
	v_mfma_f32_16x16x32_bf16 v[90:93], v[138:141], v[196:199], v[90:93]
	v_mfma_f32_16x16x32_bf16 v[78:81], v[130:133], v[204:207], v[78:81]
	v_mfma_f32_16x16x32_bf16 v[74:77], v[138:141], v[204:207], v[74:77]
	v_mfma_f32_16x16x32_bf16 v[118:121], v[146:149], v[174:177], v[118:121]
	v_mfma_f32_16x16x32_bf16 v[114:117], v[154:157], v[174:177], v[114:117]
	v_mfma_f32_16x16x32_bf16 v[102:105], v[146:149], v[188:191], v[102:105]
	v_mfma_f32_16x16x32_bf16 v[98:101], v[154:157], v[188:191], v[98:101]
	v_mfma_f32_16x16x32_bf16 v[86:89], v[146:149], v[196:199], v[86:89]
	v_mfma_f32_16x16x32_bf16 v[82:85], v[154:157], v[196:199], v[82:85]
	v_mfma_f32_16x16x32_bf16 v[70:73], v[146:149], v[204:207], v[70:73]
	v_mfma_f32_16x16x32_bf16 v[66:69], v[154:157], v[204:207], v[66:69]
	v_mfma_f32_16x16x32_bf16 v[126:129], v[134:137], v[184:187], v[126:129]
	v_mfma_f32_16x16x32_bf16 v[122:125], v[142:145], v[184:187], v[122:125]
	ds_read_b128 v[174:177], v183 offset:17408
	ds_read_b128 v[188:191], v183 offset:19456
	ds_read_b128 v[196:199], v183 offset:21504
	ds_read_b128 v[204:207], v183 offset:23552
	v_mfma_f32_16x16x32_bf16 v[110:113], v[134:137], v[192:195], v[110:113]
	v_mfma_f32_16x16x32_bf16 v[106:109], v[142:145], v[192:195], v[106:109]
	v_mfma_f32_16x16x32_bf16 v[94:97], v[134:137], v[200:203], v[94:97]
	v_mfma_f32_16x16x32_bf16 v[90:93], v[142:145], v[200:203], v[90:93]
	v_mfma_f32_16x16x32_bf16 v[78:81], v[134:137], v[216:219], v[78:81]
	v_mfma_f32_16x16x32_bf16 v[74:77], v[142:145], v[216:219], v[74:77]
	v_mfma_f32_16x16x32_bf16 v[118:121], v[150:153], v[184:187], v[118:121]
	v_mfma_f32_16x16x32_bf16 v[114:117], v[170:173], v[184:187], v[114:117]
	v_mfma_f32_16x16x32_bf16 v[102:105], v[150:153], v[192:195], v[102:105]
	v_mfma_f32_16x16x32_bf16 v[98:101], v[170:173], v[192:195], v[98:101]
	v_mfma_f32_16x16x32_bf16 v[86:89], v[150:153], v[200:203], v[86:89]
	v_mfma_f32_16x16x32_bf16 v[82:85], v[170:173], v[200:203], v[82:85]
	v_mfma_f32_16x16x32_bf16 v[70:73], v[150:153], v[216:219], v[70:73]
	v_mfma_f32_16x16x32_bf16 v[66:69], v[170:173], v[216:219], v[66:69]
	s_setprio 0
	s_setprio 1
	s_waitcnt lgkmcnt(4)
	v_mfma_f32_16x16x32_bf16 v[62:65], v[130:133], v[158:161], v[62:65]
	v_mfma_f32_16x16x32_bf16 v[58:61], v[138:141], v[158:161], v[58:61]
	v_mfma_f32_16x16x32_bf16 v[46:49], v[130:133], v[162:165], v[46:49]
	v_mfma_f32_16x16x32_bf16 v[42:45], v[138:141], v[162:165], v[42:45]
	v_mfma_f32_16x16x32_bf16 v[30:33], v[130:133], v[166:169], v[30:33]
	v_mfma_f32_16x16x32_bf16 v[26:29], v[138:141], v[166:169], v[26:29]
	v_mfma_f32_16x16x32_bf16 v[14:17], v[130:133], v[220:223], v[14:17]
	v_mfma_f32_16x16x32_bf16 v[10:13], v[138:141], v[220:223], v[10:13]
	v_mfma_f32_16x16x32_bf16 v[54:57], v[146:149], v[158:161], v[54:57]
	v_mfma_f32_16x16x32_bf16 v[50:53], v[154:157], v[158:161], v[50:53]
	v_mfma_f32_16x16x32_bf16 v[38:41], v[146:149], v[162:165], v[38:41]
	v_mfma_f32_16x16x32_bf16 v[34:37], v[154:157], v[162:165], v[34:37]
	v_mfma_f32_16x16x32_bf16 v[22:25], v[146:149], v[166:169], v[22:25]
	v_mfma_f32_16x16x32_bf16 v[18:21], v[154:157], v[166:169], v[18:21]
	v_mfma_f32_16x16x32_bf16 v[6:9], v[146:149], v[220:223], v[6:9]
	v_mfma_f32_16x16x32_bf16 v[2:5], v[154:157], v[220:223], v[2:5]
	s_waitcnt lgkmcnt(0)
	v_mfma_f32_16x16x32_bf16 v[62:65], v[134:137], v[174:177], v[62:65]
	v_mfma_f32_16x16x32_bf16 v[58:61], v[142:145], v[174:177], v[58:61]
	v_mfma_f32_16x16x32_bf16 v[46:49], v[134:137], v[188:191], v[46:49]
	v_mfma_f32_16x16x32_bf16 v[42:45], v[142:145], v[188:191], v[42:45]
	v_mfma_f32_16x16x32_bf16 v[30:33], v[134:137], v[196:199], v[30:33]
	v_mfma_f32_16x16x32_bf16 v[26:29], v[142:145], v[196:199], v[26:29]
	v_mfma_f32_16x16x32_bf16 v[14:17], v[134:137], v[204:207], v[14:17]
	v_mfma_f32_16x16x32_bf16 v[10:13], v[142:145], v[204:207], v[10:13]
	v_mfma_f32_16x16x32_bf16 v[54:57], v[150:153], v[174:177], v[54:57]
	v_mfma_f32_16x16x32_bf16 v[50:53], v[170:173], v[174:177], v[50:53]
	v_mfma_f32_16x16x32_bf16 v[38:41], v[150:153], v[188:191], v[38:41]
	v_mfma_f32_16x16x32_bf16 v[34:37], v[170:173], v[188:191], v[34:37]
	v_mfma_f32_16x16x32_bf16 v[22:25], v[150:153], v[196:199], v[22:25]
	v_mfma_f32_16x16x32_bf16 v[18:21], v[170:173], v[196:199], v[18:21]
	v_mfma_f32_16x16x32_bf16 v[6:9], v[150:153], v[204:207], v[6:9]
	v_mfma_f32_16x16x32_bf16 v[2:5], v[170:173], v[204:207], v[2:5]
	s_setprio 0
	s_waitcnt vmcnt(0)
	s_barrier
	s_add_u32 s82, s82, 0x80
	s_addc_u32 s83, s83, 0
	s_add_u32 s84, s84, 0x80
	s_addc_u32 s85, s85, 0
	s_cmp_eq_u32 s49, 7
	s_cselect_b32 s82, s40, s82
	s_cselect_b32 s83, s19, s83
	s_cselect_b32 s84, s33, s84
	s_cselect_b32 s85, s21, s85
	ds_read_b128 v[130:133], v0 offset:32768
	ds_read_b128 v[134:137], v0 offset:33792
	ds_read_b128 v[138:141], v0 offset:34816
	ds_read_b128 v[142:145], v0 offset:35840
	ds_read_b128 v[146:149], v0 offset:49152
	ds_read_b128 v[150:153], v0 offset:50176
	ds_read_b128 v[154:157], v0 offset:51200
	ds_read_b128 v[170:173], v0 offset:52224
	ds_read_b128 v[174:177], v183 offset:32768
	ds_read_b128 v[184:187], v183 offset:33792
	ds_read_b128 v[188:191], v183 offset:34816
	ds_read_b128 v[192:195], v183 offset:35840
	ds_read_b128 v[196:199], v183 offset:36864
	ds_read_b128 v[200:203], v183 offset:37888
	ds_read_b128 v[204:207], v183 offset:38912
	ds_read_b128 v[216:219], v183 offset:39936
	s_and_b64 vcc, exec, s[16:17]
	s_cbranch_vccz .Lc6x_tr_b
	s_add_u32 s26, s82, 0x10000
	s_addc_u32 s27, s83, 0
	s_add_i32 m0, s36, 0x10000
	s_nop 0
	global_load_lds_dwordx4 v208, s[82:83]
	s_add_i32 m0, s36, 0x12000
	s_nop 0
	global_load_lds_dwordx4 v209, s[82:83]
	s_add_i32 m0, s36, 0x11000
	s_nop 0
	global_load_lds_dwordx4 v208, s[26:27]
	s_add_i32 m0, s36, 0x13000
	s_nop 0
	global_load_lds_dwordx4 v209, s[26:27]
	s_add_u32 s28, s82, 0x40000
	s_addc_u32 s29, s83, 0
	s_add_u32 s26, s28, 0x10000
	s_addc_u32 s27, s29, 0
	s_add_i32 m0, s36, 0x14000
	s_nop 0
	global_load_lds_dwordx4 v208, s[28:29]
	s_add_i32 m0, s36, 0x16000
	s_nop 0
	global_load_lds_dwordx4 v209, s[28:29]
	s_add_i32 m0, s36, 0x15000
	s_nop 0
	global_load_lds_dwordx4 v208, s[26:27]
	s_add_i32 m0, s36, 0x17000
	s_nop 0
	global_load_lds_dwordx4 v209, s[26:27]
	s_add_u32 s26, s84, 0x10000
	s_addc_u32 s27, s85, 0
	s_add_i32 m0, s36, 0x0
	s_nop 0
	global_load_lds_dwordx4 v224, s[84:85]
	s_add_i32 m0, s36, 0x2000
	s_nop 0
	global_load_lds_dwordx4 v225, s[84:85]
	s_add_i32 m0, s36, 0x1000
	s_nop 0
	global_load_lds_dwordx4 v224, s[26:27]
	s_add_i32 m0, s36, 0x3000
	s_nop 0
	global_load_lds_dwordx4 v225, s[26:27]
	s_branch .Lc6x_st_b
.Lc6x_tr_b:
	s_add_u32 s28, s84, 0x40000
	s_addc_u32 s29, s85, 0
	s_add_u32 s26, s84, 0x30000
	s_addc_u32 s27, s85, 0
	s_add_i32 m0, s36, 0x4000
	s_nop 0
	global_load_lds_dwordx4 v224, s[28:29]
	s_add_i32 m0, s36, 0x6000
	s_nop 0
	global_load_lds_dwordx4 v225, s[28:29]
	s_add_i32 m0, s36, 0x3000
	s_nop 0
	global_load_lds_dwordx4 v224, s[26:27]
	s_add_i32 m0, s36, 0x5000
	s_nop 0
	global_load_lds_dwordx4 v225, s[26:27]
.Lc6x_st_b:
	s_waitcnt lgkmcnt(0)
	s_barrier
	ds_read_b128 v[158:161], v183 offset:49152
	ds_read_b128 v[162:165], v183 offset:51200
	ds_read_b128 v[166:169], v183 offset:53248
	ds_read_b128 v[220:223], v183 offset:55296
	s_setprio 1
	v_mfma_f32_16x16x32_bf16 v[126:129], v[130:133], v[174:177], v[126:129]
	v_mfma_f32_16x16x32_bf16 v[122:125], v[138:141], v[174:177], v[122:125]
	v_mfma_f32_16x16x32_bf16 v[110:113], v[130:133], v[188:191], v[110:113]
	v_mfma_f32_16x16x32_bf16 v[106:109], v[138:141], v[188:191], v[106:109]
	v_mfma_f32_16x16x32_bf16 v[94:97], v[130:133], v[196:199], v[94:97]
	v_mfma_f32_16x16x32_bf16 v[90:93], v[138:141], v[196:199], v[90:93]
	v_mfma_f32_16x16x32_bf16 v[78:81], v[130:133], v[204:207], v[78:81]
	v_mfma_f32_16x16x32_bf16 v[74:77], v[138:141], v[204:207], v[74:77]
	v_mfma_f32_16x16x32_bf16 v[118:121], v[146:149], v[174:177], v[118:121]
	v_mfma_f32_16x16x32_bf16 v[114:117], v[154:157], v[174:177], v[114:117]
	v_mfma_f32_16x16x32_bf16 v[102:105], v[146:149], v[188:191], v[102:105]
	v_mfma_f32_16x16x32_bf16 v[98:101], v[154:157], v[188:191], v[98:101]
	v_mfma_f32_16x16x32_bf16 v[86:89], v[146:149], v[196:199], v[86:89]
	v_mfma_f32_16x16x32_bf16 v[82:85], v[154:157], v[196:199], v[82:85]
	v_mfma_f32_16x16x32_bf16 v[70:73], v[146:149], v[204:207], v[70:73]
	v_mfma_f32_16x16x32_bf16 v[66:69], v[154:157], v[204:207], v[66:69]
	v_mfma_f32_16x16x32_bf16 v[126:129], v[134:137], v[184:187], v[126:129]
	v_mfma_f32_16x16x32_bf16 v[122:125], v[142:145], v[184:187], v[122:125]
	ds_read_b128 v[174:177], v183 offset:50176
	ds_read_b128 v[188:191], v183 offset:52224
	ds_read_b128 v[196:199], v183 offset:54272
	ds_read_b128 v[204:207], v183 offset:56320
	v_mfma_f32_16x16x32_bf16 v[110:113], v[134:137], v[192:195], v[110:113]
	v_mfma_f32_16x16x32_bf16 v[106:109], v[142:145], v[192:195], v[106:109]
	v_mfma_f32_16x16x32_bf16 v[94:97], v[134:137], v[200:203], v[94:97]
	v_mfma_f32_16x16x32_bf16 v[90:93], v[142:145], v[200:203], v[90:93]
	v_mfma_f32_16x16x32_bf16 v[78:81], v[134:137], v[216:219], v[78:81]
	v_mfma_f32_16x16x32_bf16 v[74:77], v[142:145], v[216:219], v[74:77]
	v_mfma_f32_16x16x32_bf16 v[118:121], v[150:153], v[184:187], v[118:121]
	v_mfma_f32_16x16x32_bf16 v[114:117], v[170:173], v[184:187], v[114:117]
	v_mfma_f32_16x16x32_bf16 v[102:105], v[150:153], v[192:195], v[102:105]
	v_mfma_f32_16x16x32_bf16 v[98:101], v[170:173], v[192:195], v[98:101]
	v_mfma_f32_16x16x32_bf16 v[86:89], v[150:153], v[200:203], v[86:89]
	v_mfma_f32_16x16x32_bf16 v[82:85], v[170:173], v[200:203], v[82:85]
	v_mfma_f32_16x16x32_bf16 v[70:73], v[150:153], v[216:219], v[70:73]
	v_mfma_f32_16x16x32_bf16 v[66:69], v[170:173], v[216:219], v[66:69]
	s_setprio 0
	s_setprio 1
	s_waitcnt lgkmcnt(4)
	v_mfma_f32_16x16x32_bf16 v[62:65], v[130:133], v[158:161], v[62:65]
	v_mfma_f32_16x16x32_bf16 v[58:61], v[138:141], v[158:161], v[58:61]
	v_mfma_f32_16x16x32_bf16 v[46:49], v[130:133], v[162:165], v[46:49]
	v_mfma_f32_16x16x32_bf16 v[42:45], v[138:141], v[162:165], v[42:45]
	v_mfma_f32_16x16x32_bf16 v[30:33], v[130:133], v[166:169], v[30:33]
	v_mfma_f32_16x16x32_bf16 v[26:29], v[138:141], v[166:169], v[26:29]
	v_mfma_f32_16x16x32_bf16 v[14:17], v[130:133], v[220:223], v[14:17]
	v_mfma_f32_16x16x32_bf16 v[10:13], v[138:141], v[220:223], v[10:13]
	v_mfma_f32_16x16x32_bf16 v[54:57], v[146:149], v[158:161], v[54:57]
	v_mfma_f32_16x16x32_bf16 v[50:53], v[154:157], v[158:161], v[50:53]
	v_mfma_f32_16x16x32_bf16 v[38:41], v[146:149], v[162:165], v[38:41]
	v_mfma_f32_16x16x32_bf16 v[34:37], v[154:157], v[162:165], v[34:37]
	v_mfma_f32_16x16x32_bf16 v[22:25], v[146:149], v[166:169], v[22:25]
	v_mfma_f32_16x16x32_bf16 v[18:21], v[154:157], v[166:169], v[18:21]
	v_mfma_f32_16x16x32_bf16 v[6:9], v[146:149], v[220:223], v[6:9]
	v_mfma_f32_16x16x32_bf16 v[2:5], v[154:157], v[220:223], v[2:5]
	s_waitcnt lgkmcnt(0)
	v_mfma_f32_16x16x32_bf16 v[62:65], v[134:137], v[174:177], v[62:65]
	v_mfma_f32_16x16x32_bf16 v[58:61], v[142:145], v[174:177], v[58:61]
	v_mfma_f32_16x16x32_bf16 v[46:49], v[134:137], v[188:191], v[46:49]
	v_mfma_f32_16x16x32_bf16 v[42:45], v[142:145], v[188:191], v[42:45]
	v_mfma_f32_16x16x32_bf16 v[30:33], v[134:137], v[196:199], v[30:33]
	v_mfma_f32_16x16x32_bf16 v[26:29], v[142:145], v[196:199], v[26:29]
	v_mfma_f32_16x16x32_bf16 v[14:17], v[134:137], v[204:207], v[14:17]
	v_mfma_f32_16x16x32_bf16 v[10:13], v[142:145], v[204:207], v[10:13]
	v_mfma_f32_16x16x32_bf16 v[54:57], v[150:153], v[174:177], v[54:57]
	v_mfma_f32_16x16x32_bf16 v[50:53], v[170:173], v[174:177], v[50:53]
	v_mfma_f32_16x16x32_bf16 v[38:41], v[150:153], v[188:191], v[38:41]
	v_mfma_f32_16x16x32_bf16 v[34:37], v[170:173], v[188:191], v[34:37]
	v_mfma_f32_16x16x32_bf16 v[22:25], v[150:153], v[196:199], v[22:25]
	v_mfma_f32_16x16x32_bf16 v[18:21], v[170:173], v[196:199], v[18:21]
	v_mfma_f32_16x16x32_bf16 v[6:9], v[150:153], v[204:207], v[6:9]
	v_mfma_f32_16x16x32_bf16 v[2:5], v[170:173], v[204:207], v[2:5]
	s_setprio 0
	s_waitcnt vmcnt(0)
	s_barrier
	s_add_i32 s49, s49, 1
	s_cmp_gt_u32 s49, 7
	s_cbranch_scc0 .LBB0_2626
	s_and_b64 vcc, exec, s[16:17]
	s_cbranch_vccz .LBB0_2629
	s_barrier
